# MLA fast88 loop: dead zero-initialisations of the bf8 P registers removed (both pack halves are written), on top of hoist + deferred PV MFMA
# speedup vs baseline: 1.0044x; 1.0044x over previous
; __device__ __forceinline__ bool mla_unit_fast88(const Args& A, int b, int h, int qb, ALAS char* shm, const int tidb) {
;     ...
;                 {
;                     ALAS const char* Ks_ = Kfr + ks1 * KSLOT;
;                     v8i kfa, kfb; M8_KFRAG(kfa, Ks_, 0, 0);
;                     M8_KFRAG(kfb, Ks_, 0, 1);
;                     mfma8_new(N0, kfa, qf0, negm, sa8, sb8);
; #pragma unroll
;                     for (int e = 0; e < 8; ++e) C0[e] = __builtin_amdgcn_exp2f(C0[e]);
;                     __builtin_amdgcn_sched_barrier(0);
;                     M8_KFRAG(kfa, Ks_, 1, 0);
;                     mfma8_new(N1, kfb, qf0, negm, sa8, sb8);
; #pragma unroll
;                     for (int e = 8; e < 16; ++e) C0[e] = __builtin_amdgcn_exp2f(C0[e]);
;                     __builtin_amdgcn_sched_barrier(0);
;                     M8_KFRAG(kfb, Ks_, 1, 1);
;                     mfma8_acc(N0, kfa, qf1, sa8, sb8);
; #pragma unroll
;                     for (int e = 0; e < 8; ++e) C1[e] = __builtin_amdgcn_exp2f(C1[e]);
;                     __builtin_amdgcn_sched_barrier(0);
;                     mfma8_acc(N1, kfb, qf1, sa8, sb8);
; #pragma unroll
;                     for (int e = 8; e < 16; ++e) C1[e] = __builtin_amdgcn_exp2f(C1[e]);
;                     __builtin_amdgcn_sched_barrier(0);
;                 }
;                 ALAS const char* vb_ = shm + L_V + vs * 4096 + lane * 16;
;                 v8i vf0, vf1;
;                 { const u32x4 a0 = *(ALAS const u32x4*)(vb_), a1 = *(ALAS const u32x4*)(vb_ + 1024), b0 = *(ALAS const u32x4*)(vb_ + 2048), b1 = *(ALAS const u32x4*)(vb_ + 3072);
;                   vf0 = (v8i){(int)a0.x, (int)a0.y, (int)a0.z, (int)a0.w, (int)a1.x, (int)a1.y, (int)a1.z, (int)a1.w}; vf1 = (v8i){(int)b0.x, (int)b0.y, (int)b0.z, (int)b0.w, (int)b1.x, (int)b1.y, (int)b1.z, (int)b1.w}; }
;                 v8i pf;
; #pragma unroll
;                 for (int kk = 0; kk < 4; ++kk) { const f32x16& cc_ = (kk < 2) ? C0 : C1; const int k8_ = 8 * (kk & 1);
;                     int w0_ = 0, w1_ = 0;
;                     w0_ = __builtin_amdgcn_cvt_pk_bf8_f32(cc_[k8_], cc_[k8_ + 1], w0_, false); w0_ = __builtin_amdgcn_cvt_pk_bf8_f32(cc_[k8_ + 2], cc_[k8_ + 3], w0_, true);
;                     w1_ = __builtin_amdgcn_cvt_pk_bf8_f32(cc_[k8_ + 4], cc_[k8_ + 5], w1_, false); w1_ = __builtin_amdgcn_cvt_pk_bf8_f32(cc_[k8_ + 6], cc_[k8_ + 7], w1_, true);
.LBB0_653:
	s_add_i32 s7, s5, -3
	s_cmp_gt_i32 s7, s47
	s_cbranch_scc1 .Lmla_nv0
	v_lshl_add_u32 v158, s4, 13, v157
	v_exp_f32_e32 v50, v50
	v_exp_f32_e32 v51, v51
	v_exp_f32_e32 v52, v52
	v_exp_f32_e32 v53, v53
	v_exp_f32_e32 v54, v54
	v_exp_f32_e32 v55, v55
	v_exp_f32_e32 v56, v56
	v_exp_f32_e32 v57, v57
	s_waitcnt lgkmcnt(2)
	v_mfma_scale_f32_32x32x64_f8f6f4 v[98:113], v[114:121], v[130:137], v[66:81], v247, v253 op_sel_hi:[0,0,0]
	ds_read_b128 v[172:175], v158 offset:4096
	ds_read_b128 v[176:179], v158 offset:5120
	v_exp_f32_e32 v58, v58
	v_exp_f32_e32 v59, v59
	v_exp_f32_e32 v60, v60
	v_exp_f32_e32 v61, v61
	v_exp_f32_e32 v62, v62
	v_exp_f32_e32 v63, v63
	v_exp_f32_e32 v64, v64
	v_exp_f32_e32 v65, v65
	s_waitcnt lgkmcnt(2)
	v_mfma_scale_f32_32x32x64_f8f6f4 v[114:129], v[164:171], v[130:137], v[66:81], v247, v253 op_sel_hi:[0,0,0]
	ds_read_b128 v[164:167], v158 offset:6144
	ds_read_b128 v[168:171], v158 offset:7168
	v_exp_f32_e32 v82, v82
	v_exp_f32_e32 v83, v83
	v_exp_f32_e32 v84, v84
	v_exp_f32_e32 v85, v85
	v_exp_f32_e32 v86, v86
	v_exp_f32_e32 v87, v87
	v_exp_f32_e32 v88, v88
	v_exp_f32_e32 v89, v89
	s_waitcnt lgkmcnt(2)
	v_mfma_scale_f32_32x32x64_f8f6f4 v[98:113], v[172:179], v[138:145], v[98:113], v247, v253 op_sel_hi:[0,0,0]
	v_exp_f32_e32 v90, v90
	v_exp_f32_e32 v91, v91
	v_exp_f32_e32 v92, v92
	v_exp_f32_e32 v93, v93
	v_exp_f32_e32 v94, v94
	v_exp_f32_e32 v95, v95
	v_exp_f32_e32 v96, v96
	v_exp_f32_e32 v97, v97
	s_waitcnt lgkmcnt(0)
	v_mfma_scale_f32_32x32x64_f8f6f4 v[114:129], v[164:171], v[138:145], v[114:129], v247, v253 op_sel_hi:[0,0,0]
	ds_read_b128 v[164:167], v157 offset:36864
	ds_read_b128 v[168:171], v157 offset:37888
	ds_read_b128 v[172:175], v157 offset:38912
	ds_read_b128 v[176:179], v157 offset:39936
	v_cvt_pk_bf8_f32 v180, v50, v51
	v_cvt_pk_bf8_f32 v181, v54, v55
	v_cvt_pk_bf8_f32 v182, v58, v59
	v_cvt_pk_bf8_f32 v183, v62, v63
	v_cvt_pk_bf8_f32 v184, v82, v83
	v_cvt_pk_bf8_f32 v185, v86, v87
	v_cvt_pk_bf8_f32 v186, v90, v91
	v_cvt_pk_bf8_f32 v187, v94, v95
	v_cvt_pk_bf8_f32 v180, v52, v53 op_sel:[0,0,1]
	v_cvt_pk_bf8_f32 v181, v56, v57 op_sel:[0,0,1]
	v_cvt_pk_bf8_f32 v182, v60, v61 op_sel:[0,0,1]
	v_cvt_pk_bf8_f32 v183, v64, v65 op_sel:[0,0,1]
	v_cvt_pk_bf8_f32 v184, v84, v85 op_sel:[0,0,1]
	v_cvt_pk_bf8_f32 v185, v88, v89 op_sel:[0,0,1]
	v_cvt_pk_bf8_f32 v186, v92, v93 op_sel:[0,0,1]
	v_cvt_pk_bf8_f32 v187, v96, v97 op_sel:[0,0,1]
	s_waitcnt lgkmcnt(2)
	v_mfma_scale_f32_32x32x64_f8f6f4 v[2:17], v[180:187], v[164:171], v[2:17], v251, v247 op_sel_hi:[0,0,0] cbsz:1
	s_waitcnt lgkmcnt(0)
	v_mov_b32_e32 v163, v162
	v_mov_b32_e32 v164, v162
	v_mov_b32_e32 v165, v162
	v_mov_b32_e32 v166, v162
	v_mov_b32_e32 v167, v162
	v_mov_b32_e32 v168, v162
	v_mov_b32_e32 v169, v162
	v_mfma_scale_f32_32x32x64_f8f6f4 v[34:49], v[180:187], v[162:169], v[34:49], v251, v251 op_sel_hi:[0,0,0] cbsz:1

; __device__ __forceinline__ bool mla_unit_fast88(const Args& A, int b, int h, int qb, ALAS char* shm, const int tidb) {
;     ...
;                 {
;                     ALAS const char* Ks_ = Kfr + ks1 * KSLOT;
;                     v8i kfa, kfb; M8_KFRAG(kfa, Ks_, 0, 0);
;                     M8_KFRAG(kfb, Ks_, 0, 1);
;                     mfma8_new(N0, kfa, qf0, negm, sa8, sb8);
; #pragma unroll
;                     for (int e = 0; e < 8; ++e) C0[e] = __builtin_amdgcn_exp2f(C0[e]);
;                     __builtin_amdgcn_sched_barrier(0);
;                     M8_KFRAG(kfa, Ks_, 1, 0);
;                     mfma8_new(N1, kfb, qf0, negm, sa8, sb8);
; #pragma unroll
;                     for (int e = 8; e < 16; ++e) C0[e] = __builtin_amdgcn_exp2f(C0[e]);
;                     __builtin_amdgcn_sched_barrier(0);
;                     M8_KFRAG(kfb, Ks_, 1, 1);
;                     mfma8_acc(N0, kfa, qf1, sa8, sb8);
; #pragma unroll
;                     for (int e = 0; e < 8; ++e) C1[e] = __builtin_amdgcn_exp2f(C1[e]);
;                     __builtin_amdgcn_sched_barrier(0);
;                     mfma8_acc(N1, kfb, qf1, sa8, sb8);
; #pragma unroll
;                     for (int e = 8; e < 16; ++e) C1[e] = __builtin_amdgcn_exp2f(C1[e]);
;                     __builtin_amdgcn_sched_barrier(0);
;                 }
;                 ALAS const char* vb_ = shm + L_V + vs * 4096 + lane * 16;
;                 v8i vf0, vf1;
;                 { const u32x4 a0 = *(ALAS const u32x4*)(vb_), a1 = *(ALAS const u32x4*)(vb_ + 1024), b0 = *(ALAS const u32x4*)(vb_ + 2048), b1 = *(ALAS const u32x4*)(vb_ + 3072);
;                   vf0 = (v8i){(int)a0.x, (int)a0.y, (int)a0.z, (int)a0.w, (int)a1.x, (int)a1.y, (int)a1.z, (int)a1.w}; vf1 = (v8i){(int)b0.x, (int)b0.y, (int)b0.z, (int)b0.w, (int)b1.x, (int)b1.y, (int)b1.z, (int)b1.w}; }
;                 v8i pf;
; #pragma unroll
;                 for (int kk = 0; kk < 4; ++kk) { const f32x16& cc_ = (kk < 2) ? C0 : C1; const int k8_ = 8 * (kk & 1);
;                     int w0_ = 0, w1_ = 0;
;                     w0_ = __builtin_amdgcn_cvt_pk_bf8_f32(cc_[k8_], cc_[k8_ + 1], w0_, false); w0_ = __builtin_amdgcn_cvt_pk_bf8_f32(cc_[k8_ + 2], cc_[k8_ + 3], w0_, true);
;                     w1_ = __builtin_amdgcn_cvt_pk_bf8_f32(cc_[k8_ + 4], cc_[k8_ + 5], w1_, false); w1_ = __builtin_amdgcn_cvt_pk_bf8_f32(cc_[k8_ + 6], cc_[k8_ + 7], w1_, true);
.LBB0_658:
	v_lshl_add_u32 v146, s4, 13, v157
	v_exp_f32_e32 v98, v98
	v_exp_f32_e32 v99, v99
	v_exp_f32_e32 v100, v100
	v_exp_f32_e32 v101, v101
	v_exp_f32_e32 v102, v102
	v_exp_f32_e32 v103, v103
	v_exp_f32_e32 v104, v104
	v_exp_f32_e32 v105, v105
	s_waitcnt lgkmcnt(2)
	v_mfma_scale_f32_32x32x64_f8f6f4 v[50:65], v[82:89], v[130:137], v[66:81], v247, v253 op_sel_hi:[0,0,0]
	ds_read_b128 v[172:175], v146 offset:4096
	ds_read_b128 v[176:179], v146 offset:5120
	v_exp_f32_e32 v106, v106
	v_exp_f32_e32 v107, v107
	v_exp_f32_e32 v108, v108
	v_exp_f32_e32 v109, v109
	v_exp_f32_e32 v110, v110
	v_exp_f32_e32 v111, v111
	v_exp_f32_e32 v112, v112
	v_exp_f32_e32 v113, v113
	s_waitcnt lgkmcnt(2)
	v_mfma_scale_f32_32x32x64_f8f6f4 v[82:97], v[164:171], v[130:137], v[66:81], v247, v253 op_sel_hi:[0,0,0]
	ds_read_b128 v[164:167], v146 offset:6144
	ds_read_b128 v[168:171], v146 offset:7168
	v_exp_f32_e32 v114, v114
	v_exp_f32_e32 v115, v115
	v_exp_f32_e32 v116, v116
	v_exp_f32_e32 v117, v117
	v_exp_f32_e32 v118, v118
	v_exp_f32_e32 v119, v119
	v_exp_f32_e32 v120, v120
	v_exp_f32_e32 v121, v121
	s_waitcnt lgkmcnt(2)
	v_mfma_scale_f32_32x32x64_f8f6f4 v[50:65], v[172:179], v[138:145], v[50:65], v247, v253 op_sel_hi:[0,0,0]
	v_exp_f32_e32 v122, v122
	v_exp_f32_e32 v123, v123
	v_exp_f32_e32 v124, v124
	v_exp_f32_e32 v125, v125
	v_exp_f32_e32 v126, v126
	v_exp_f32_e32 v127, v127
	v_exp_f32_e32 v128, v128
	v_exp_f32_e32 v129, v129
	s_waitcnt lgkmcnt(0)
	v_mfma_scale_f32_32x32x64_f8f6f4 v[82:97], v[164:171], v[138:145], v[82:97], v247, v253 op_sel_hi:[0,0,0]
	ds_read_b128 v[164:167], v157 offset:40960
	ds_read_b128 v[168:171], v157 offset:41984
	ds_read_b128 v[172:175], v157 offset:43008
	ds_read_b128 v[176:179], v157 offset:44032
	v_cvt_pk_bf8_f32 v180, v98, v99
	v_cvt_pk_bf8_f32 v181, v102, v103
	v_cvt_pk_bf8_f32 v182, v106, v107
	v_cvt_pk_bf8_f32 v183, v110, v111
	v_cvt_pk_bf8_f32 v184, v114, v115
	v_cvt_pk_bf8_f32 v185, v118, v119
	v_cvt_pk_bf8_f32 v186, v122, v123
	v_cvt_pk_bf8_f32 v187, v126, v127
	v_cvt_pk_bf8_f32 v180, v100, v101 op_sel:[0,0,1]
	v_cvt_pk_bf8_f32 v181, v104, v105 op_sel:[0,0,1]
	v_cvt_pk_bf8_f32 v182, v108, v109 op_sel:[0,0,1]
	v_cvt_pk_bf8_f32 v183, v112, v113 op_sel:[0,0,1]
	v_cvt_pk_bf8_f32 v184, v116, v117 op_sel:[0,0,1]
	v_cvt_pk_bf8_f32 v185, v120, v121 op_sel:[0,0,1]
	v_cvt_pk_bf8_f32 v186, v124, v125 op_sel:[0,0,1]
	v_cvt_pk_bf8_f32 v187, v128, v129 op_sel:[0,0,1]
	s_waitcnt lgkmcnt(2)
	v_mfma_scale_f32_32x32x64_f8f6f4 v[2:17], v[180:187], v[164:171], v[2:17], v251, v247 op_sel_hi:[0,0,0] cbsz:1
	s_waitcnt lgkmcnt(0)
	v_mov_b32_e32 v163, v162
	v_mov_b32_e32 v164, v162
	v_mov_b32_e32 v165, v162
	v_mov_b32_e32 v166, v162
	v_mov_b32_e32 v167, v162
	v_mov_b32_e32 v168, v162
	v_mov_b32_e32 v169, v162
	v_mfma_scale_f32_32x32x64_f8f6f4 v[34:49], v[180:187], v[162:169], v[34:49], v251, v251 op_sel_hi:[0,0,0] cbsz:1
